# attention units pulled from a global counter by every workgroup at the end of the scan phase (dynamic balancing with the RWKV / mLSTM chains)
# speedup vs baseline: 1.0115x; 1.0115x over previous
; #define PH(k, ...) do { if (IN(pb + (k))) { { __VA_ARGS__ } if ((MK_DUP >> (k)) & 1) { xcd_barrier(bar); { __VA_ARGS__ } } } SEAM(pb + (k)); } while (0)
; template <int l> DI void run_layer(const Args& A, LAS unsigned char* lds, const XcdBarrier& bar, int lo, int hi, int G, int bid, int tid, int lane, int wave, int gw, int ngw, int gtid, int nthr) {
;     ...
;     PH(3,
;           if (G > ATT_SCAN_BLK0 && bid >= ATT_SCAN_BLK0) phase_attn(A, lds, 0, ATT_UNITS - ATT_SPLIT, bid - ATT_SCAN_BLK0, G - ATT_SCAN_BLK0, tid, wave, lane);
;           for (int rep = 0; rep < 1 + ((MK_DUP >> 14) & 1); ++rep) for (int u = bid; u < 96; u += G) rwkv_r2_unit(A, lds, u, tid, wave, lane);
;           for (int rep = 0; rep < 1 + ((MK_DUP >> 15) & 1); ++rep) for (int u = bid; u < 96 + 64; u += G) { if (u >= 96) mlstm_m2_unit(A, lds, u - 96, tid, wave, lane); });
.LBB0_546:
	s_cmp_lt_i32 s6, 5
	s_cselect_b64 s[94:95], -1, 0
	s_and_b64 s[0:1], s[94:95], s[0:1]
	s_andn2_b64 vcc, exec, s[0:1]
	s_cbranch_vccnz .LBB0_957
	s_cmpk_lt_i32 s50, 0xa1
	s_cselect_b64 s[0:1], -1, 0
	s_cmpk_lt_i32 s92, 0xa0
	s_cselect_b64 s[2:3], -1, 0
	s_or_b64 s[0:1], s[2:3], s[0:1]
	s_and_b64 vcc, exec, s[0:1]
	s_cbranch_vccnz .LBB0_640
	s_add_i32 s22, s92, 0xffffff60
	s_cmpk_gt_u32 s22, 0x23f
	s_cbranch_scc1 .LBB0_639
	s_branch .LBB0_639

; #define LAS __attribute__((address_space(3)))
; DI void attn_unit(const Args& A, LAS unsigned char* lds, int unit, int tid, int wave, int lane) {
;     const bf16* Z = (const bf16*)(A.ws + WS_Z); bf16* ao = (bf16*)(A.ws + WS_ATTO); float* al = (float*)(A.ws + WS_ATTL);
;     const int x = unit & 15; int r0 = unit >> 4; const int hh = r0 & 3; r0 >>= 2; const int b = r0 % NB, br = r0 / NB;
;     const int dil = br == 0 ? 1 : (br == 1 ? 4 : 16), lsub = SEQ / dil, nblk = lsub / 128;
;     const int res = x / nblk, nbk = x % nblk, l0 = nbk * 128, wbase = l0 - 64;
;     LAS bf16* Qs = (LAS bf16*)(lds + AT_QS); LAS bf16* Ks = (LAS bf16*)(lds + AT_KS); LAS bf16* Vt = (LAS bf16*)(lds + AT_VT); LAS float* btab = (LAS float*)(lds + AT_BT);
;     __syncthreads();
; #pragma unroll
;     for (int i = 0; i < 2; ++i) { const int id = tid + 512 * i, row = id >> 3, ch = id & 7; const int tok = b * SEQ + (l0 + row) * dil + res;
;         *(LAS u32x4_t*)(Qs + row * AT_QLD + ch * 8) = *(const u32x4_t*)(Z + (size_t)tok * ZLD + ZA + hh * 64 + ch * 8); }
;     for (int id = tid; id < 272 * 8; id += NTHR) { const int row = id >> 3, ch = id & 7; const int pos = wbase + row; u32x4_t v = (u32x4_t){0u, 0u, 0u, 0u};
;         if (row < 256 && pos >= 0 && pos < lsub) v = *(const u32x4_t*)(Z + (size_t)(b * SEQ + pos * dil + res) * ZLD + ZA + 256 + hh * 64 + ch * 8);
;         *(LAS u32x4_t*)(Ks + row * AT_QLD + ch * 8) = v; }
;     for (int id = tid; id < 272 * 8; id += NTHR) { const int key = id % 272, ch = id / 272; const int pos = wbase + key; u32x4_t v = (u32x4_t){0u, 0u, 0u, 0u};
;         if (key < 256 && pos >= 0 && pos < lsub) v = *(const u32x4_t*)(Z + (size_t)(b * SEQ + pos * dil + res) * ZLD + ZA + 512 + hh * 64 + ch * 8);
;         LAS bf16* d = Vt + (ch * 8) * AT_VLD + key;
;         d[0] = (bf16)(v.x & 0xffffu); d[AT_VLD] = (bf16)(v.x >> 16); d[2 * AT_VLD] = (bf16)(v.y & 0xffffu); d[3 * AT_VLD] = (bf16)(v.y >> 16);
;         d[4 * AT_VLD] = (bf16)(v.z & 0xffffu); d[5 * AT_VLD] = (bf16)(v.z >> 16); d[6 * AT_VLD] = (bf16)(v.w & 0xffffu); d[7 * AT_VLD] = (bf16)(v.w >> 16); }
;     if (tid < 129) btab[tid] = A.in[I_RELB][t5_bucket((tid - 64) * dil) * 4 + hh] * 1.4426950408889634f;
;     __syncthreads();
.LBB0_957:
	v_readlane_b32 s9, v235, 52
	v_readlane_b32 s2, v235, 9
	v_readlane_b32 s3, v235, 10
	v_readlane_b32 s4, v235, 19
	v_readlane_b32 s5, v235, 20
	s_mov_b32 s72, 0x3e38aa3b
	s_mov_b32 s73, 0x3e38aa3b
	v_lshrrev_b32_e32 v2, 3, v0
	v_and_b32_e32 v3, 7, v0
	v_lshlrev_b32_e32 v3, 4, v3
	s_movk_i32 s39, 0x90
	v_mad_u32_u24 v1, v2, s39, v3
	v_and_b32_e32 v5, 0xff, v0
	v_lshrrev_b32_e32 v6, 8, v0
	s_movk_i32 s39, 0x1180
	v_mul_u32_u24_e32 v4, s39, v6
	v_lshl_add_u32 v4, v5, 1, v4
	v_add_u32_e32 v4, 0xe100, v4
	v_lshlrev_b32_e32 v6, 4, v6
	v_lshlrev_b32_e32 v8, 2, v5
	v_add_u32_e32 v8, 0x16d00, v8
	v_subrev_u32_e32 v165, 16, v0
	s_movk_i32 s39, 0x81
	v_cmp_gt_u32_e64 s[42:43], s39, v165
	s_movk_i32 s39, 0xa0
	v_cmp_gt_u32_e64 s[48:49], s39, v0
	v_cmp_gt_u32_e64 s[46:47], 64, v0
	v_cmp_gt_u32_e64 s[44:45], 16, v146
	v_subrev_u32_e32 v165, 0x50, v0
	v_cmp_lt_i32_e32 vcc, 0, v165
	v_mov_b32_e32 v7, 0
	s_nop 0
	v_cndmask_b32_e64 v166, 0, 16, vcc
	v_lshlrev_b32_e32 v167, 0, v165
	v_sub_u32_e32 v168, 0, v167
	v_max_i32_e32 v167, v167, v168
	v_cvt_f32_u32_e32 v168, v167
	v_mul_f32_e32 v168, 0x3e000000, v168
	v_max_f32_e32 v168, 1.0, v168
	v_log_f32_e32 v168, v168
	v_cmp_gt_u32_e32 vcc, 8, v167
	v_mul_f32_e32 v168, 0x3f924925, v168
	v_cvt_i32_f32_e32 v168, v168
	v_min_i32_e32 v168, 7, v168
	v_add_u32_e32 v168, 8, v168
	v_cndmask_b32_e32 v168, v168, v167, vcc
	v_add_u32_e32 v168, v168, v166
	v_lshl_or_b32 v7, v168, 0, v7
	v_lshlrev_b32_e32 v167, 2, v165
	v_sub_u32_e32 v168, 0, v167
	v_max_i32_e32 v167, v167, v168
	v_cvt_f32_u32_e32 v168, v167
	v_mul_f32_e32 v168, 0x3e000000, v168
	v_max_f32_e32 v168, 1.0, v168
	v_log_f32_e32 v168, v168
	v_cmp_gt_u32_e32 vcc, 8, v167
	v_mul_f32_e32 v168, 0x3f924925, v168
	v_cvt_i32_f32_e32 v168, v168
	v_min_i32_e32 v168, 7, v168
	v_add_u32_e32 v168, 8, v168
	v_cndmask_b32_e32 v168, v168, v167, vcc
	v_add_u32_e32 v168, v168, v166
	v_lshl_or_b32 v7, v168, 8, v7
	v_lshlrev_b32_e32 v167, 4, v165
	v_sub_u32_e32 v168, 0, v167
	v_max_i32_e32 v167, v167, v168
	v_cvt_f32_u32_e32 v168, v167
	v_mul_f32_e32 v168, 0x3e000000, v168
	v_max_f32_e32 v168, 1.0, v168
	v_log_f32_e32 v168, v168
	v_cmp_gt_u32_e32 vcc, 8, v167
	v_mul_f32_e32 v168, 0x3f924925, v168
	v_cvt_i32_f32_e32 v168, v168
	v_min_i32_e32 v168, 7, v168
	v_add_u32_e32 v168, 8, v168
	v_cndmask_b32_e32 v168, v168, v167, vcc
	v_add_u32_e32 v168, v168, v166
	v_lshl_or_b32 v7, v168, 16, v7
	v_and_b32_e32 v165, 15, v146
	v_lshrrev_b32_e32 v166, 4, v146
	s_lshl_b32 s39, s9, 4
	v_add_u32_e32 v40, s39, v165
	s_movk_i32 s40, 0x90
	v_mul_u32_u24_e32 v34, s40, v40
	v_lshl_add_u32 v34, v166, 4, v34
	v_lshlrev_b32_e32 v167, 2, v166
	v_sub_u32_e32 v35, v167, v165
	v_lshlrev_b32_e32 v35, 2, v35
	v_add_u32_e32 v35, 0x16d40, v35
	v_add_u32_e32 v167, s39, v167
	v_lshlrev_b32_e32 v36, 2, v167
	v_add_u32_e32 v36, 0x16f80, v36
	s_movk_i32 s40, 0x230
	v_mul_u32_u24_e32 v37, s40, v165
	v_lshl_add_u32 v37, v167, 1, v37
	v_add_u32_e32 v37, 0xe100, v37
	v_add_u32_e32 v9, 0x2300, v37
	v_add_u32_e32 v118, 0x4600, v37
	v_add_u32_e32 v144, 0x6900, v37
	v_xor_b32_e32 v38, 16, v146
	v_lshlrev_b32_e32 v38, 2, v38
	v_xor_b32_e32 v39, 32, v146
	v_lshlrev_b32_e32 v39, 2, v39
	v_lshlrev_b32_e32 v41, 3, v166
	v_mov_b32_e32 v232, 0
	v_mov_b32_e32 v233, 0
	s_movk_i32 s40, 0x230
	v_mul_u32_u24_e32 v168, s40, v0
	v_add_u32_e32 v168, 0xe300, v168
	s_and_saveexec_b64 s[40:41], s[46:47]
	ds_write_b64 v168, v[232:233] offset:0
	ds_write_b64 v168, v[232:233] offset:8
	ds_write_b64 v168, v[232:233] offset:16
	ds_write_b64 v168, v[232:233] offset:24
	s_mov_b64 exec, s[40:41]
	s_add_u32 s88, s2, 0x20000
	s_addc_u32 s89, s3, 0
	s_mov_b32 s90, 0x600
	s_cmp_lg_u32 s9, 0
	s_cbranch_scc1 .LatE_w1
	s_mov_b64 exec, 1
	v_mov_b32_e32 v11, 0
	v_mov_b32_e32 v10, 2
	global_atomic_add v10, v11, v10, s[88:89] sc0
	v_mov_b32_e32 v12, 0x23fa0
	s_waitcnt vmcnt(0)
	ds_write_b32 v12, v10
	s_mov_b64 exec, -1
.LatE_w1:
	s_waitcnt lgkmcnt(0)
	s_barrier
	v_mov_b32_e32 v12, 0x23fa0
	ds_read_b32 v13, v12
	s_waitcnt lgkmcnt(0)
	v_readfirstlane_b32 s6, v13
	s_nop 3
	s_add_i32 s90, s6, 1
	s_movk_i32 s8, 0x600
	s_cmp_lt_i32 s6, s8
	s_cbranch_scc0 .LatE_done
	s_cmp_lg_u32 s9, 0
	s_cbranch_scc1 .LatE_w2
	s_mov_b64 exec, 1
	v_mov_b32_e32 v10, 1
	global_atomic_add v10, v11, v10, s[88:89] sc0
	s_mov_b64 exec, -1
.LatE_w2:
	s_and_b32 s39, s6, 15
	s_bfe_u32 s40, s6, 0x20004
	s_bfe_u32 s41, s6, 0x30006
	s_lshr_b32 s74, s6, 9
	s_lshl_b32 s75, s74, 1
	s_add_i32 s16, s75, 13
	s_add_i32 s20, s75, 9
	s_add_i32 s26, s75, 4
	s_lshl_b32 s28, s74, 3
	s_lshr_b32 s29, 0x800, s75
	s_add_i32 s17, s29, -1
	s_sub_i32 s76, 4, s75
	s_lshr_b32 s77, s39, s76
	s_lshr_b32 s78, 16, s75
	s_add_i32 s78, s78, -1
	s_and_b32 s78, s39, s78
	s_lshl_b32 s19, s78, 7
	s_add_i32 s18, s19, 0xffffffc0
	s_lshl_b32 s79, s41, 11
	s_add_i32 s79, s79, s77
	s_lshl_b32 s80, s40, 7
	s_lshl_b32 s27, s40, 2
	s_lshl_b32 s81, s79, 13
	s_add_u32 s81, s81, s80
	s_add_u32 s81, s81, 0x2ca00000
	s_add_u32 s10, s2, s81
	s_addc_u32 s11, s3, 0
	s_lshl_b32 s82, s74, 14
	s_add_i32 s82, s82, s79
	s_lshl_b32 s83, s82, 9
	s_add_u32 s83, s83, s80
	s_add_u32 s83, s83, 0x34a00000
	s_add_u32 s12, s2, s83
	s_addc_u32 s13, s3, 0
	s_lshl_b32 s84, s82, 4
	s_add_u32 s84, s84, s27
	s_add_u32 s84, s84, 0x36200000
	s_add_u32 s14, s2, s84
	s_addc_u32 s15, s3, 0
	v_add_u32_e32 v165, s19, v2
	v_lshl_add_u32 v165, v165, s16, v3
	s_lshl_b32 s85, 64, s16
	global_load_dwordx4 v[120:123], v165, s[10:11]
	v_add_u32_e32 v166, s85, v165
	global_load_dwordx4 v[124:127], v166, s[10:11]
	v_add_u32_e32 v167, s18, v2
	v_med3_i32 v168, v167, 0, s17
	v_lshl_add_u32 v168, v168, s16, v3
	global_load_dwordx4 v[128:131], v168, s[10:11] offset:512
	v_add_u32_e32 v168, 64, v167
	v_med3_i32 v168, v168, 0, s17
	v_lshl_add_u32 v168, v168, s16, v3
	global_load_dwordx4 v[132:135], v168, s[10:11] offset:512
	v_add_u32_e32 v168, 0x80, v167
	v_med3_i32 v168, v168, 0, s17
	v_lshl_add_u32 v168, v168, s16, v3
	global_load_dwordx4 v[136:139], v168, s[10:11] offset:512
	v_add_u32_e32 v168, 0xc0, v167
	v_med3_i32 v168, v168, 0, s17
	v_lshl_add_u32 v168, v168, s16, v3
	global_load_dwordx4 v[140:143], v168, s[10:11] offset:512
	v_add_u32_e32 v169, s18, v5
	v_med3_i32 v169, v169, 0, s17
	v_lshl_add_u32 v169, v169, s16, v6
	global_load_dwordx4 v[148:151], v169, s[10:11] offset:1024
	global_load_dwordx4 v[152:155], v169, s[10:11] offset:1056
	global_load_dwordx4 v[156:159], v169, s[10:11] offset:1088
	global_load_dwordx4 v[160:163], v169, s[10:11] offset:1120
	v_bfe_u32 v171, v7, s28, 8
	v_lshl_add_u32 v171, v171, 4, s27
	s_mov_b64 exec, s[42:43]
	global_load_dword v164, v171, s[4:5]
	s_mov_b64 exec, -1
; #define LAS __attribute__((address_space(3)))
; DI void attn_unit(const Args& A, LAS unsigned char* lds, int unit, int tid, int wave, int lane) {
;     ...
;     __syncthreads();
; #pragma unroll
;     for (int i = 0; i < 2; ++i) { const int id = tid + 512 * i, row = id >> 3, ch = id & 7; const int tok = b * SEQ + (l0 + row) * dil + res;
;         *(LAS u32x4_t*)(Qs + row * AT_QLD + ch * 8) = *(const u32x4_t*)(Z + (size_t)tok * ZLD + ZA + hh * 64 + ch * 8); }
;     for (int id = tid; id < 272 * 8; id += NTHR) { const int row = id >> 3, ch = id & 7; const int pos = wbase + row; u32x4_t v = (u32x4_t){0u, 0u, 0u, 0u};
;         if (row < 256 && pos >= 0 && pos < lsub) v = *(const u32x4_t*)(Z + (size_t)(b * SEQ + pos * dil + res) * ZLD + ZA + 256 + hh * 64 + ch * 8);
;         *(LAS u32x4_t*)(Ks + row * AT_QLD + ch * 8) = v; }
;     for (int id = tid; id < 272 * 8; id += NTHR) { const int key = id % 272, ch = id / 272; const int pos = wbase + key; u32x4_t v = (u32x4_t){0u, 0u, 0u, 0u};
;         if (key < 256 && pos >= 0 && pos < lsub) v = *(const u32x4_t*)(Z + (size_t)(b * SEQ + pos * dil + res) * ZLD + ZA + 512 + hh * 64 + ch * 8);
;         LAS bf16* d = Vt + (ch * 8) * AT_VLD + key;
;         d[0] = (bf16)(v.x & 0xffffu); d[AT_VLD] = (bf16)(v.x >> 16); d[2 * AT_VLD] = (bf16)(v.y & 0xffffu); d[3 * AT_VLD] = (bf16)(v.y >> 16);
;         d[4 * AT_VLD] = (bf16)(v.z & 0xffffu); d[5 * AT_VLD] = (bf16)(v.z >> 16); d[6 * AT_VLD] = (bf16)(v.w & 0xffffu); d[7 * AT_VLD] = (bf16)(v.w >> 16); }
;     if (tid < 129) btab[tid] = A.in[I_RELB][t5_bucket((tid - 64) * dil) * 4 + hh] * 1.4426950408889634f;
;     __syncthreads();
.LatE_loop:
	s_barrier
	s_mov_b64 s[30:31], s[12:13]
	s_mov_b64 s[32:33], s[14:15]
	s_mov_b32 s34, s19
	s_mov_b32 s35, s20
	s_mov_b32 s36, s26
	s_mov_b32 s37, s18
	s_mov_b32 s38, s29
	v_add_u32_e32 v165, s37, v5
	v_cmp_gt_u32_e32 vcc, s38, v165
	v_mov_b32_e32 v166, 0xf149f2ca
	s_nop 0
	v_cndmask_b32_e64 v165, v166, 0, vcc
	ds_write_b32 v8, v165 offset:640
	s_waitcnt vmcnt(0)
	ds_write_b128 v1, v[120:123]
	ds_write_b128 v1, v[124:127] offset:9216
	ds_write_b128 v1, v[128:131] offset:18432
	ds_write_b128 v1, v[132:135] offset:27648
	ds_write_b128 v1, v[136:139] offset:36864
	ds_write_b128 v1, v[140:143] offset:46080
	ds_write_b16 v4, v148 offset:0
	ds_write_b16_d16_hi v4, v148 offset:560
	ds_write_b16 v4, v149 offset:1120
	ds_write_b16_d16_hi v4, v149 offset:1680
	ds_write_b16 v4, v150 offset:2240
	ds_write_b16_d16_hi v4, v150 offset:2800
	ds_write_b16 v4, v151 offset:3360
	ds_write_b16_d16_hi v4, v151 offset:3920
	ds_write_b16 v4, v152 offset:8960
	ds_write_b16_d16_hi v4, v152 offset:9520
	ds_write_b16 v4, v153 offset:10080
	ds_write_b16_d16_hi v4, v153 offset:10640
	ds_write_b16 v4, v154 offset:11200
	ds_write_b16_d16_hi v4, v154 offset:11760
	ds_write_b16 v4, v155 offset:12320
	ds_write_b16_d16_hi v4, v155 offset:12880
	ds_write_b16 v4, v156 offset:17920
	ds_write_b16_d16_hi v4, v156 offset:18480
	ds_write_b16 v4, v157 offset:19040
	ds_write_b16_d16_hi v4, v157 offset:19600
	ds_write_b16 v4, v158 offset:20160
	ds_write_b16_d16_hi v4, v158 offset:20720
	ds_write_b16 v4, v159 offset:21280
	ds_write_b16_d16_hi v4, v159 offset:21840
	ds_write_b16 v4, v160 offset:26880
	ds_write_b16_d16_hi v4, v160 offset:27440
	ds_write_b16 v4, v161 offset:28000
	ds_write_b16_d16_hi v4, v161 offset:28560
	ds_write_b16 v4, v162 offset:29120
	ds_write_b16_d16_hi v4, v162 offset:29680
	ds_write_b16 v4, v163 offset:30240
	ds_write_b16_d16_hi v4, v163 offset:30800
	v_mul_f32_e32 v167, 0x3fb8aa3b, v164
	v_cndmask_b32_e64 v167, v166, v167, s[42:43]
	s_mov_b64 exec, s[48:49]
	ds_write_b32 v8, v167
	s_mov_b64 exec, -1
	s_cmp_lg_u32 s9, 0
	s_cbranch_scc1 .LatE_w3
	s_mov_b64 exec, 1
	v_mov_b32_e32 v12, 0x23fa0
	ds_write_b32 v12, v10
	s_nop 1
	v_mov_b32_e32 v10, 1
	global_atomic_add v10, v11, v10, s[88:89] sc0
	s_mov_b64 exec, -1
.LatE_w3:
	s_mov_b32 s6, s90
	s_cmp_lt_i32 s6, s8
	s_cbranch_scc0 .LatE_nopf
	s_and_b32 s39, s6, 15
	s_bfe_u32 s40, s6, 0x20004
	s_bfe_u32 s41, s6, 0x30006
	s_lshr_b32 s74, s6, 9
	s_lshl_b32 s75, s74, 1
	s_add_i32 s16, s75, 13
	s_add_i32 s20, s75, 9
	s_add_i32 s26, s75, 4
	s_lshl_b32 s28, s74, 3
	s_lshr_b32 s29, 0x800, s75
	s_add_i32 s17, s29, -1
	s_sub_i32 s76, 4, s75
	s_lshr_b32 s77, s39, s76
	s_lshr_b32 s78, 16, s75
	s_add_i32 s78, s78, -1
	s_and_b32 s78, s39, s78
	s_lshl_b32 s19, s78, 7
	s_add_i32 s18, s19, 0xffffffc0
	s_lshl_b32 s79, s41, 11
	s_add_i32 s79, s79, s77
	s_lshl_b32 s80, s40, 7
	s_lshl_b32 s27, s40, 2
	s_lshl_b32 s81, s79, 13
	s_add_u32 s81, s81, s80
	s_add_u32 s81, s81, 0x2ca00000
	s_add_u32 s10, s2, s81
	s_addc_u32 s11, s3, 0
	s_lshl_b32 s82, s74, 14
	s_add_i32 s82, s82, s79
	s_lshl_b32 s83, s82, 9
	s_add_u32 s83, s83, s80
	s_add_u32 s83, s83, 0x34a00000
	s_add_u32 s12, s2, s83
	s_addc_u32 s13, s3, 0
	s_lshl_b32 s84, s82, 4
	s_add_u32 s84, s84, s27
	s_add_u32 s84, s84, 0x36200000
	s_add_u32 s14, s2, s84
	s_addc_u32 s15, s3, 0
	v_add_u32_e32 v165, s19, v2
	v_lshl_add_u32 v165, v165, s16, v3
	s_lshl_b32 s85, 64, s16
	global_load_dwordx4 v[120:123], v165, s[10:11]
	v_add_u32_e32 v166, s85, v165
	global_load_dwordx4 v[124:127], v166, s[10:11]
	v_add_u32_e32 v167, s18, v2
	v_med3_i32 v168, v167, 0, s17
	v_lshl_add_u32 v168, v168, s16, v3
	global_load_dwordx4 v[128:131], v168, s[10:11] offset:512
	v_add_u32_e32 v168, 64, v167
	v_med3_i32 v168, v168, 0, s17
	v_lshl_add_u32 v168, v168, s16, v3
	global_load_dwordx4 v[132:135], v168, s[10:11] offset:512
	v_add_u32_e32 v168, 0x80, v167
	v_med3_i32 v168, v168, 0, s17
	v_lshl_add_u32 v168, v168, s16, v3
	global_load_dwordx4 v[136:139], v168, s[10:11] offset:512
	v_add_u32_e32 v168, 0xc0, v167
	v_med3_i32 v168, v168, 0, s17
	v_lshl_add_u32 v168, v168, s16, v3
	global_load_dwordx4 v[140:143], v168, s[10:11] offset:512
	v_add_u32_e32 v169, s18, v5
	v_med3_i32 v169, v169, 0, s17
	v_lshl_add_u32 v169, v169, s16, v6
	global_load_dwordx4 v[148:151], v169, s[10:11] offset:1024
	global_load_dwordx4 v[152:155], v169, s[10:11] offset:1056
	global_load_dwordx4 v[156:159], v169, s[10:11] offset:1088
	global_load_dwordx4 v[160:163], v169, s[10:11] offset:1120
	v_bfe_u32 v171, v7, s28, 8
	v_lshl_add_u32 v171, v171, 4, s27
	s_mov_b64 exec, s[42:43]
	global_load_dword v164, v171, s[4:5]
	s_mov_b64 exec, -1
; #define LAS __attribute__((address_space(3)))
; #define MFMA16(a, b, c) __builtin_amdgcn_mfma_f32_16x16x32_bf16((a), (b), (c), 0, 0, 0)
; DI void attn_unit(const Args& A, LAS unsigned char* lds, int unit, int tid, int wave, int lane) {
;     ...
;     const int fr = lane & 15, qd = lane >> 4;
;     f32x4 acc[10];
;     { bf16x8_t qb[2];
; #pragma unroll
;       for (int ks = 0; ks < 2; ++ks) qb[ks] = *(const LAS bf16x8_t*)(Qs + (16 * wave + fr) * AT_QLD + ks * 32 + 8 * qd);
; #pragma unroll
;       for (int j = 0; j < 10; ++j) { acc[j] = (f32x4){0.f, 0.f, 0.f, 0.f};
;           if (j == 9) continue;
; #pragma unroll
;           for (int ks = 0; ks < 2; ++ks) { const bf16x8_t ka = *(const LAS bf16x8_t*)(Ks + (16 * (wave + j) + fr) * AT_QLD + ks * 32 + 8 * qd); acc[j] = MFMA16(ka, qb[ks], acc[j]); } } }
;     const int iq = 16 * wave + fr; float mx = -1.0e30f;
;     int dv[4];
; #pragma unroll
;     for (int r = 0; r < 4; ++r) dv[r] = 4 * qd + r - fr;
;     const int p0 = wbase + 16 * wave + 4 * qd;
; #pragma unroll
;     for (int j = 0; j < 9; ++j)
; #pragma unroll
;         for (int r = 0; r < 4; ++r) { const int t = 16 * j + dv[r]; bool valid = (unsigned)(p0 + 16 * j + r) < (unsigned)lsub;
;             if (j == 0) valid = valid && (dv[r] >= 0); if (j == 8) valid = valid && (dv[r] <= 0);
;             const int ti = (j == 0) ? (t < 0 ? 0 : t) : ((j == 8) ? (t > 128 ? 128 : t) : t);
;             const float s = valid ? acc[j][r] * (0.125f * 1.4426950408889634f) + btab[ti] : -1.0e30f; acc[j][r] = s; mx = fmaxf(mx, s); }
.LatE_nopf:
	s_waitcnt lgkmcnt(0)
	s_barrier
	v_mov_b32_e32 v12, 0x23fa0
	ds_read_b32 v13, v12
	s_waitcnt lgkmcnt(0)
	v_readfirstlane_b32 s90, v13
	ds_read_b128 v[172:175], v34
	ds_read_b128 v[176:179], v34 offset:64
	ds_read_b128 v[216:219], v34 offset:18432
	ds_read_b128 v[220:223], v34 offset:18496
	ds_read_b128 v[224:227], v34 offset:20736
	ds_read_b128 v[228:231], v34 offset:20800
	ds_read_b128 v[236:239], v34 offset:23040
	ds_read_b128 v[240:243], v34 offset:23104
	ds_read_b128 v[244:247], v34 offset:25344
	ds_read_b128 v[248:251], v34 offset:25408
	ds_read_b128 v[110:113], v34 offset:27648
	ds_read_b128 v[114:117], v34 offset:27712
	s_waitcnt lgkmcnt(8)
	v_mfma_f32_16x16x32_bf16 v[180:183], v[216:219], v[172:175], 0
	v_mfma_f32_16x16x32_bf16 v[180:183], v[220:223], v[176:179], v[180:183]
	ds_read_b128 v[216:219], v34 offset:29952
	ds_read_b128 v[220:223], v34 offset:30016
	s_waitcnt lgkmcnt(8)
	v_mfma_f32_16x16x32_bf16 v[184:187], v[224:227], v[172:175], 0
	v_mfma_f32_16x16x32_bf16 v[184:187], v[228:231], v[176:179], v[184:187]
	ds_read_b128 v[224:227], v34 offset:32256
	ds_read_b128 v[228:231], v34 offset:32320
	s_waitcnt lgkmcnt(8)
	v_mfma_f32_16x16x32_bf16 v[188:191], v[236:239], v[172:175], 0
	v_mfma_f32_16x16x32_bf16 v[188:191], v[240:243], v[176:179], v[188:191]
	ds_read_b128 v[236:239], v34 offset:34560
	ds_read_b128 v[240:243], v34 offset:34624
	s_waitcnt lgkmcnt(8)
	v_mfma_f32_16x16x32_bf16 v[192:195], v[244:247], v[172:175], 0
	v_mfma_f32_16x16x32_bf16 v[192:195], v[248:251], v[176:179], v[192:195]
	ds_read_b128 v[244:247], v34 offset:36864
	ds_read_b128 v[248:251], v34 offset:36928
	s_waitcnt lgkmcnt(8)
	v_mfma_f32_16x16x32_bf16 v[196:199], v[110:113], v[172:175], 0
	v_mfma_f32_16x16x32_bf16 v[196:199], v[114:117], v[176:179], v[196:199]
	s_waitcnt lgkmcnt(6)
	v_mfma_f32_16x16x32_bf16 v[200:203], v[216:219], v[172:175], 0
	v_mfma_f32_16x16x32_bf16 v[200:203], v[220:223], v[176:179], v[200:203]
	s_waitcnt lgkmcnt(4)
	v_mfma_f32_16x16x32_bf16 v[204:207], v[224:227], v[172:175], 0
	v_mfma_f32_16x16x32_bf16 v[204:207], v[228:231], v[176:179], v[204:207]
	s_waitcnt lgkmcnt(2)
	v_mfma_f32_16x16x32_bf16 v[208:211], v[236:239], v[172:175], 0
	v_mfma_f32_16x16x32_bf16 v[208:211], v[240:243], v[176:179], v[208:211]
	s_waitcnt lgkmcnt(0)
	v_mfma_f32_16x16x32_bf16 v[212:215], v[244:247], v[172:175], 0
	v_mfma_f32_16x16x32_bf16 v[212:215], v[248:251], v[176:179], v[212:215]
	s_nop 7
	ds_read2_b32 v[216:217], v35 offset0:0 offset1:1
	ds_read2_b32 v[218:219], v35 offset0:2 offset1:3
	ds_read_b128 v[220:223], v36 offset:0
	ds_read2_b32 v[224:225], v35 offset0:16 offset1:17
	ds_read2_b32 v[226:227], v35 offset0:18 offset1:19
	ds_read_b128 v[228:231], v36 offset:64
	ds_read2_b32 v[236:237], v35 offset0:32 offset1:33
	ds_read2_b32 v[238:239], v35 offset0:34 offset1:35
	ds_read_b128 v[240:243], v36 offset:128
	ds_read2_b32 v[244:245], v35 offset0:48 offset1:49
	ds_read2_b32 v[246:247], v35 offset0:50 offset1:51
	ds_read_b128 v[248:251], v36 offset:192
	v_mov_b32_e32 v46, 0xf149f2ca
	s_waitcnt lgkmcnt(9)
	v_pk_fma_f32 v[180:181], v[180:181], s[72:73], v[216:217]
	v_pk_fma_f32 v[182:183], v[182:183], s[72:73], v[218:219]
	v_pk_add_f32 v[180:181], v[180:181], v[220:221]
	v_pk_add_f32 v[182:183], v[182:183], v[222:223]
	v_max3_f32 v46, v46, v180, v181
	v_max3_f32 v46, v46, v182, v183
	ds_read2_b32 v[216:217], v35 offset0:64 offset1:65
	ds_read2_b32 v[218:219], v35 offset0:66 offset1:67
	ds_read_b128 v[220:223], v36 offset:256
	s_waitcnt lgkmcnt(9)
	v_pk_fma_f32 v[184:185], v[184:185], s[72:73], v[224:225]
	v_pk_fma_f32 v[186:187], v[186:187], s[72:73], v[226:227]
	v_pk_add_f32 v[184:185], v[184:185], v[228:229]
	v_pk_add_f32 v[186:187], v[186:187], v[230:231]
	v_max3_f32 v46, v46, v184, v185
	v_max3_f32 v46, v46, v186, v187
	ds_read2_b32 v[224:225], v35 offset0:80 offset1:81
	ds_read2_b32 v[226:227], v35 offset0:82 offset1:83
	ds_read_b128 v[228:231], v36 offset:320
	s_waitcnt lgkmcnt(9)
	v_pk_fma_f32 v[188:189], v[188:189], s[72:73], v[236:237]
	v_pk_fma_f32 v[190:191], v[190:191], s[72:73], v[238:239]
	v_pk_add_f32 v[188:189], v[188:189], v[240:241]
	v_pk_add_f32 v[190:191], v[190:191], v[242:243]
	v_max3_f32 v46, v46, v188, v189
	v_max3_f32 v46, v46, v190, v191
	ds_read2_b32 v[236:237], v35 offset0:96 offset1:97
	ds_read2_b32 v[238:239], v35 offset0:98 offset1:99
	ds_read_b128 v[240:243], v36 offset:384
	s_waitcnt lgkmcnt(9)
	v_pk_fma_f32 v[192:193], v[192:193], s[72:73], v[244:245]
	v_pk_fma_f32 v[194:195], v[194:195], s[72:73], v[246:247]
	v_pk_add_f32 v[192:193], v[192:193], v[248:249]
	v_pk_add_f32 v[194:195], v[194:195], v[250:251]
	v_max3_f32 v46, v46, v192, v193
	v_max3_f32 v46, v46, v194, v195
	ds_read2_b32 v[244:245], v35 offset0:112 offset1:113
	ds_read2_b32 v[246:247], v35 offset0:114 offset1:115
	ds_read_b128 v[248:251], v36 offset:448
	s_waitcnt lgkmcnt(9)
	v_pk_fma_f32 v[196:197], v[196:197], s[72:73], v[216:217]
	v_pk_fma_f32 v[198:199], v[198:199], s[72:73], v[218:219]
	v_pk_add_f32 v[196:197], v[196:197], v[220:221]
	v_pk_add_f32 v[198:199], v[198:199], v[222:223]
	v_max3_f32 v46, v46, v196, v197
	v_max3_f32 v46, v46, v198, v199
	ds_read2_b32 v[216:217], v35 offset0:128 offset1:129
	ds_read2_b32 v[218:219], v35 offset0:130 offset1:131
	ds_read_b128 v[220:223], v36 offset:512
	s_waitcnt lgkmcnt(9)
	v_pk_fma_f32 v[200:201], v[200:201], s[72:73], v[224:225]
	v_pk_fma_f32 v[202:203], v[202:203], s[72:73], v[226:227]
	v_pk_add_f32 v[200:201], v[200:201], v[228:229]
	v_pk_add_f32 v[202:203], v[202:203], v[230:231]
	v_max3_f32 v46, v46, v200, v201
	v_max3_f32 v46, v46, v202, v203
	s_waitcnt lgkmcnt(6)
; #define LAS __attribute__((address_space(3)))
; DI unsigned cvtpk(float lo, float hi) { const f2_t v = {lo, hi}; return __builtin_bit_cast(unsigned, __builtin_convertvector(v, bf2_t)); }
; #define MFMA16(a, b, c) __builtin_amdgcn_mfma_f32_16x16x32_bf16((a), (b), (c), 0, 0, 0)
; DI void attn_unit(const Args& A, LAS unsigned char* lds, int unit, int tid, int wave, int lane) {
;     ...
;     mx = fmaxf(mx, __shfl_xor(mx, 16)); mx = fmaxf(mx, __shfl_xor(mx, 32));
;     float lsum = 0.f;
; #pragma unroll
;     for (int j = 0; j < 9; ++j)
; #pragma unroll
;         for (int r = 0; r < 4; ++r) { const float p = __builtin_amdgcn_exp2f(acc[j][r] - mx); acc[j][r] = p; lsum += p; }
;     lsum += __shfl_xor(lsum, 16); lsum += __shfl_xor(lsum, 32);
;     f32x4 oacc[4];
; #pragma unroll
;     for (int d = 0; d < 4; ++d) oacc[d] = (f32x4){0.f, 0.f, 0.f, 0.f};
; #pragma unroll
;     for (int pp = 0; pp < 5; ++pp) {
;         union { unsigned u[4]; bf16x8_t v; } pb;
;         pb.u[0] = cvtpk(acc[2 * pp][0], acc[2 * pp][1]); pb.u[1] = cvtpk(acc[2 * pp][2], acc[2 * pp][3]); pb.u[2] = cvtpk(acc[2 * pp + 1][0], acc[2 * pp + 1][1]); pb.u[3] = cvtpk(acc[2 * pp + 1][2], acc[2 * pp + 1][3]);
; #pragma unroll
;         for (int d = 0; d < 4; ++d) { const LAS bf16* vp = Vt + (16 * d + fr) * AT_VLD + 16 * (wave + 2 * pp) + 4 * qd;
;             union { bf16x4_t h[2]; bf16x8_t v; } va; va.h[0] = *(const LAS bf16x4_t*)vp; va.h[1] = *(const LAS bf16x4_t*)(vp + 16);
;             oacc[d] = MFMA16(va.v, pb.v, oacc[d]); } }
	v_pk_fma_f32 v[204:205], v[204:205], s[72:73], v[236:237]
	v_pk_fma_f32 v[206:207], v[206:207], s[72:73], v[238:239]
	v_pk_add_f32 v[204:205], v[204:205], v[240:241]
	v_pk_add_f32 v[206:207], v[206:207], v[242:243]
	v_max3_f32 v46, v46, v204, v205
	v_max3_f32 v46, v46, v206, v207
	s_waitcnt lgkmcnt(3)
	v_pk_fma_f32 v[208:209], v[208:209], s[72:73], v[244:245]
	v_pk_fma_f32 v[210:211], v[210:211], s[72:73], v[246:247]
	v_pk_add_f32 v[208:209], v[208:209], v[248:249]
	v_pk_add_f32 v[210:211], v[210:211], v[250:251]
	v_max3_f32 v46, v46, v208, v209
	v_max3_f32 v46, v46, v210, v211
	s_waitcnt lgkmcnt(0)
	s_nop 4
	v_pk_fma_f32 v[212:213], v[212:213], s[72:73], v[216:217]
	v_pk_fma_f32 v[214:215], v[214:215], s[72:73], v[218:219]
	v_pk_add_f32 v[212:213], v[212:213], v[220:221]
	v_pk_add_f32 v[214:215], v[214:215], v[222:223]
	v_max3_f32 v46, v46, v212, v213
	v_max3_f32 v46, v46, v214, v215
	ds_bpermute_b32 v165, v38, v46
	s_waitcnt lgkmcnt(0)
	v_max_f32_e32 v46, v46, v165
	s_nop 0
	ds_bpermute_b32 v165, v39, v46
	s_waitcnt lgkmcnt(0)
	v_max_f32_e32 v46, v46, v165
	ds_read2_b64 v[216:219], v37 offset0:0 offset1:4
	ds_read2_b64 v[220:223], v9 offset0:0 offset1:4
	ds_read2_b64 v[224:227], v118 offset0:0 offset1:4
	ds_read2_b64 v[228:231], v144 offset0:0 offset1:4
	ds_read2_b64 v[236:239], v37 offset0:8 offset1:12
	ds_read2_b64 v[240:243], v9 offset0:8 offset1:12
	ds_read2_b64 v[244:247], v118 offset0:8 offset1:12
	ds_read2_b64 v[248:251], v144 offset0:8 offset1:12
	v_mov_b32_e32 v47, v46
	v_pk_add_f32 v[180:181], v[180:181], v[46:47] neg_lo:[0,1] neg_hi:[0,1]
	v_pk_add_f32 v[182:183], v[182:183], v[46:47] neg_lo:[0,1] neg_hi:[0,1]
	v_pk_add_f32 v[184:185], v[184:185], v[46:47] neg_lo:[0,1] neg_hi:[0,1]
	v_pk_add_f32 v[186:187], v[186:187], v[46:47] neg_lo:[0,1] neg_hi:[0,1]
	v_pk_add_f32 v[188:189], v[188:189], v[46:47] neg_lo:[0,1] neg_hi:[0,1]
	v_pk_add_f32 v[190:191], v[190:191], v[46:47] neg_lo:[0,1] neg_hi:[0,1]
	v_pk_add_f32 v[192:193], v[192:193], v[46:47] neg_lo:[0,1] neg_hi:[0,1]
	v_pk_add_f32 v[194:195], v[194:195], v[46:47] neg_lo:[0,1] neg_hi:[0,1]
	v_pk_add_f32 v[196:197], v[196:197], v[46:47] neg_lo:[0,1] neg_hi:[0,1]
	v_pk_add_f32 v[198:199], v[198:199], v[46:47] neg_lo:[0,1] neg_hi:[0,1]
	v_pk_add_f32 v[200:201], v[200:201], v[46:47] neg_lo:[0,1] neg_hi:[0,1]
	v_pk_add_f32 v[202:203], v[202:203], v[46:47] neg_lo:[0,1] neg_hi:[0,1]
	v_pk_add_f32 v[204:205], v[204:205], v[46:47] neg_lo:[0,1] neg_hi:[0,1]
	v_pk_add_f32 v[206:207], v[206:207], v[46:47] neg_lo:[0,1] neg_hi:[0,1]
	v_pk_add_f32 v[208:209], v[208:209], v[46:47] neg_lo:[0,1] neg_hi:[0,1]
	v_pk_add_f32 v[210:211], v[210:211], v[46:47] neg_lo:[0,1] neg_hi:[0,1]
	v_pk_add_f32 v[212:213], v[212:213], v[46:47] neg_lo:[0,1] neg_hi:[0,1]
	v_pk_add_f32 v[214:215], v[214:215], v[46:47] neg_lo:[0,1] neg_hi:[0,1]
	v_exp_f32_e32 v180, v180
	v_exp_f32_e32 v181, v181
	v_exp_f32_e32 v182, v182
	v_add_f32_e32 v145, 0, v180
	v_exp_f32_e32 v183, v183
	v_add_f32_e32 v145, v181, v145
	v_exp_f32_e32 v184, v184
	v_add_f32_e32 v145, v182, v145
	v_exp_f32_e32 v185, v185
	v_add_f32_e32 v145, v183, v145
	v_exp_f32_e32 v186, v186
	v_add_f32_e32 v145, v184, v145
	v_exp_f32_e32 v187, v187
	v_add_f32_e32 v145, v185, v145
	v_exp_f32_e32 v188, v188
	v_add_f32_e32 v145, v186, v145
	v_exp_f32_e32 v189, v189
	v_add_f32_e32 v145, v187, v145
	v_exp_f32_e32 v190, v190
	v_add_f32_e32 v145, v188, v145
	v_exp_f32_e32 v191, v191
	v_add_f32_e32 v145, v189, v145
	v_exp_f32_e32 v192, v192
	v_add_f32_e32 v145, v190, v145
	v_exp_f32_e32 v193, v193
	v_add_f32_e32 v145, v191, v145
	v_exp_f32_e32 v194, v194
	v_add_f32_e32 v145, v192, v145
	v_exp_f32_e32 v195, v195
	v_add_f32_e32 v145, v193, v145
	v_exp_f32_e32 v196, v196
	v_add_f32_e32 v145, v194, v145
	v_exp_f32_e32 v197, v197
	v_add_f32_e32 v145, v195, v145
	v_exp_f32_e32 v198, v198
	v_add_f32_e32 v145, v196, v145
	v_exp_f32_e32 v199, v199
	v_add_f32_e32 v145, v197, v145
	v_exp_f32_e32 v200, v200
	v_add_f32_e32 v145, v198, v145
	v_exp_f32_e32 v201, v201
	v_add_f32_e32 v145, v199, v145
	v_exp_f32_e32 v202, v202
	v_add_f32_e32 v145, v200, v145
	v_exp_f32_e32 v203, v203
	v_add_f32_e32 v145, v201, v145
	v_exp_f32_e32 v204, v204
	v_add_f32_e32 v145, v202, v145
	v_exp_f32_e32 v205, v205
	v_add_f32_e32 v145, v203, v145
	v_exp_f32_e32 v206, v206
	v_add_f32_e32 v145, v204, v145
	v_exp_f32_e32 v207, v207
	v_add_f32_e32 v145, v205, v145
	v_exp_f32_e32 v208, v208
	v_add_f32_e32 v145, v206, v145
	v_exp_f32_e32 v209, v209
	v_add_f32_e32 v145, v207, v145
	v_exp_f32_e32 v210, v210
	v_add_f32_e32 v145, v208, v145
	v_exp_f32_e32 v211, v211
	v_add_f32_e32 v145, v209, v145
	v_exp_f32_e32 v212, v212
	v_add_f32_e32 v145, v210, v145
	v_exp_f32_e32 v213, v213
	v_add_f32_e32 v145, v211, v145
	v_exp_f32_e32 v214, v214
	v_add_f32_e32 v145, v212, v145
	v_exp_f32_e32 v215, v215
	v_add_f32_e32 v145, v213, v145
	s_nop 0
	v_add_f32_e32 v145, v214, v145
	v_add_f32_e32 v145, v215, v145
	v_cvt_pk_bf16_f32 v110, v180, v181
	v_cvt_pk_bf16_f32 v111, v182, v183
	v_cvt_pk_bf16_f32 v112, v184, v185
	v_cvt_pk_bf16_f32 v113, v186, v187
	s_nop 1
	s_waitcnt lgkmcnt(7)
	v_mfma_f32_16x16x32_bf16 v[172:175], v[216:219], v[110:113], 0
	ds_read2_b64 v[216:219], v37 offset0:16 offset1:20
	s_waitcnt lgkmcnt(7)
	v_mfma_f32_16x16x32_bf16 v[176:179], v[220:223], v[110:113], 0
	ds_read2_b64 v[220:223], v9 offset0:16 offset1:20
	s_waitcnt lgkmcnt(7)
; #define LAS __attribute__((address_space(3)))
; DI unsigned cvtpk(float lo, float hi) { const f2_t v = {lo, hi}; return __builtin_bit_cast(unsigned, __builtin_convertvector(v, bf2_t)); }
; #define MFMA16(a, b, c) __builtin_amdgcn_mfma_f32_16x16x32_bf16((a), (b), (c), 0, 0, 0)
; DI void attn_unit(const Args& A, LAS unsigned char* lds, int unit, int tid, int wave, int lane) {
;     ...
; #pragma unroll
;     for (int pp = 0; pp < 5; ++pp) {
;         union { unsigned u[4]; bf16x8_t v; } pb;
;         pb.u[0] = cvtpk(acc[2 * pp][0], acc[2 * pp][1]); pb.u[1] = cvtpk(acc[2 * pp][2], acc[2 * pp][3]); pb.u[2] = cvtpk(acc[2 * pp + 1][0], acc[2 * pp + 1][1]); pb.u[3] = cvtpk(acc[2 * pp + 1][2], acc[2 * pp + 1][3]);
; #pragma unroll
;         for (int d = 0; d < 4; ++d) { const LAS bf16* vp = Vt + (16 * d + fr) * AT_VLD + 16 * (wave + 2 * pp) + 4 * qd;
;             union { bf16x4_t h[2]; bf16x8_t v; } va; va.h[0] = *(const LAS bf16x4_t*)vp; va.h[1] = *(const LAS bf16x4_t*)(vp + 16);
;             oacc[d] = MFMA16(va.v, pb.v, oacc[d]); } }
;     const float inv = 1.f / lsum; const int tok = b * SEQ + (l0 + iq) * dil + res;
;     bf16* op = ao + ((size_t)br * NT + tok) * AW + hh * 64 + 4 * qd;
; #pragma unroll
;     for (int d = 0; d < 4; ++d) { uint2 w; w.x = cvtpk(oacc[d][0] * inv, oacc[d][1] * inv); w.y = cvtpk(oacc[d][2] * inv, oacc[d][3] * inv); *(uint2*)(op + 16 * d) = w; }
;     if (qd == 0) al[((size_t)br * NT + tok) * 4 + hh] = mx * 0.6931471805599453f + logf(lsum);
	v_mfma_f32_16x16x32_bf16 v[114:117], v[224:227], v[110:113], 0
	ds_read2_b64 v[224:227], v118 offset0:16 offset1:20
	s_waitcnt lgkmcnt(7)
	v_mfma_f32_16x16x32_bf16 v[252:255], v[228:231], v[110:113], 0
	ds_read2_b64 v[228:231], v144 offset0:16 offset1:20
	v_cvt_pk_bf16_f32 v42, v188, v189
	v_cvt_pk_bf16_f32 v43, v190, v191
	v_cvt_pk_bf16_f32 v44, v192, v193
	v_cvt_pk_bf16_f32 v45, v194, v195
	s_nop 1
	s_waitcnt lgkmcnt(7)
	v_mfma_f32_16x16x32_bf16 v[172:175], v[236:239], v[42:45], v[172:175]
	ds_read2_b64 v[236:239], v37 offset0:24 offset1:28
	s_waitcnt lgkmcnt(7)
	v_mfma_f32_16x16x32_bf16 v[176:179], v[240:243], v[42:45], v[176:179]
	ds_read2_b64 v[240:243], v9 offset0:24 offset1:28
	s_waitcnt lgkmcnt(7)
	v_mfma_f32_16x16x32_bf16 v[114:117], v[244:247], v[42:45], v[114:117]
	ds_read2_b64 v[244:247], v118 offset0:24 offset1:28
	s_waitcnt lgkmcnt(7)
	v_mfma_f32_16x16x32_bf16 v[252:255], v[248:251], v[42:45], v[252:255]
	ds_read2_b64 v[248:251], v144 offset0:24 offset1:28
	v_cvt_pk_bf16_f32 v110, v196, v197
	v_cvt_pk_bf16_f32 v111, v198, v199
	v_cvt_pk_bf16_f32 v112, v200, v201
	v_cvt_pk_bf16_f32 v113, v202, v203
	s_nop 1
	s_waitcnt lgkmcnt(7)
	v_mfma_f32_16x16x32_bf16 v[172:175], v[216:219], v[110:113], v[172:175]
	ds_read2_b64 v[216:219], v37 offset0:32 offset1:36
	s_waitcnt lgkmcnt(7)
	v_mfma_f32_16x16x32_bf16 v[176:179], v[220:223], v[110:113], v[176:179]
	ds_read2_b64 v[220:223], v9 offset0:32 offset1:36
	s_waitcnt lgkmcnt(7)
	v_mfma_f32_16x16x32_bf16 v[114:117], v[224:227], v[110:113], v[114:117]
	ds_read2_b64 v[224:227], v118 offset0:32 offset1:36
	s_waitcnt lgkmcnt(7)
	v_mfma_f32_16x16x32_bf16 v[252:255], v[228:231], v[110:113], v[252:255]
	ds_read2_b64 v[228:231], v144 offset0:32 offset1:36
	v_cvt_pk_bf16_f32 v42, v204, v205
	v_cvt_pk_bf16_f32 v43, v206, v207
	v_cvt_pk_bf16_f32 v44, v208, v209
	v_cvt_pk_bf16_f32 v45, v210, v211
	s_nop 1
	s_waitcnt lgkmcnt(7)
	v_mfma_f32_16x16x32_bf16 v[172:175], v[236:239], v[42:45], v[172:175]
	s_waitcnt lgkmcnt(6)
	v_mfma_f32_16x16x32_bf16 v[176:179], v[240:243], v[42:45], v[176:179]
	s_waitcnt lgkmcnt(5)
	v_mfma_f32_16x16x32_bf16 v[114:117], v[244:247], v[42:45], v[114:117]
	s_waitcnt lgkmcnt(4)
	v_mfma_f32_16x16x32_bf16 v[252:255], v[248:251], v[42:45], v[252:255]
	v_cvt_pk_bf16_f32 v110, v212, v213
	v_cvt_pk_bf16_f32 v111, v214, v215
	v_mov_b32_e32 v112, 0
	v_mov_b32_e32 v113, 0
	s_nop 1
	s_waitcnt lgkmcnt(3)
	v_mfma_f32_16x16x32_bf16 v[172:175], v[216:219], v[110:113], v[172:175]
	s_waitcnt lgkmcnt(2)
	v_mfma_f32_16x16x32_bf16 v[176:179], v[220:223], v[110:113], v[176:179]
	s_waitcnt lgkmcnt(1)
	v_mfma_f32_16x16x32_bf16 v[114:117], v[224:227], v[110:113], v[114:117]
	s_waitcnt lgkmcnt(0)
	v_mfma_f32_16x16x32_bf16 v[252:255], v[228:231], v[110:113], v[252:255]
	ds_bpermute_b32 v165, v38, v145
	v_add_u32_e32 v167, s34, v40
	v_lshl_add_u32 v168, v167, s35, v41
	v_lshlrev_b32_e32 v167, s36, v167
	s_waitcnt lgkmcnt(0)
	v_add_f32_e32 v145, v145, v165
	s_nop 0
	ds_bpermute_b32 v165, v39, v145
	s_waitcnt lgkmcnt(0)
	v_add_f32_e32 v169, v145, v165
	v_div_scale_f32 v165, s[40:41], v169, v169, 1.0
	v_rcp_f32_e32 v166, v165
	s_nop 0
	v_fma_f32 v171, -v165, v166, 1.0
	v_fmac_f32_e32 v166, v171, v166
	v_div_scale_f32 v171, vcc, 1.0, v169, 1.0
	v_mul_f32_e32 v232, v171, v166
	v_fma_f32 v233, -v165, v232, v171
	v_fmac_f32_e32 v232, v233, v166
	v_fma_f32 v165, -v165, v232, v171
	s_nop 1
	v_div_fmas_f32 v165, v165, v166, v232
	v_div_fixup_f32 v165, v165, v169, 1.0
	v_mul_f32_e32 v172, v165, v172
	v_mul_f32_e32 v173, v165, v173
	v_mul_f32_e32 v174, v165, v174
	v_mul_f32_e32 v175, v165, v175
	v_cvt_pk_bf16_f32 v172, v172, v173
	v_cvt_pk_bf16_f32 v173, v174, v175
	global_store_dwordx2 v168, v[172:173], s[30:31] offset:0
	v_mul_f32_e32 v176, v165, v176
	v_mul_f32_e32 v177, v165, v177
	v_mul_f32_e32 v178, v165, v178
	v_mul_f32_e32 v179, v165, v179
	v_cvt_pk_bf16_f32 v176, v176, v177
	v_cvt_pk_bf16_f32 v177, v178, v179
	global_store_dwordx2 v168, v[176:177], s[30:31] offset:32
	v_mul_f32_e32 v114, v165, v114
	v_mul_f32_e32 v115, v165, v115
	v_mul_f32_e32 v116, v165, v116
	v_mul_f32_e32 v117, v165, v117
	v_cvt_pk_bf16_f32 v114, v114, v115
	v_cvt_pk_bf16_f32 v115, v116, v117
	global_store_dwordx2 v168, v[114:115], s[30:31] offset:64
	v_mul_f32_e32 v252, v165, v252
	v_mul_f32_e32 v253, v165, v253
	v_mul_f32_e32 v254, v165, v254
	v_mul_f32_e32 v255, v165, v255
	v_cvt_pk_bf16_f32 v252, v252, v253
	v_cvt_pk_bf16_f32 v253, v254, v255
	global_store_dwordx2 v168, v[252:253], s[30:31] offset:96
	s_mov_b32 s39, 0x800000
	v_cmp_gt_f32_e32 vcc, s39, v169
	v_mov_b32_e32 v232, 0x41b17218
	s_nop 0
	v_cndmask_b32_e64 v166, 0, 32, vcc
	v_ldexp_f32 v169, v169, v166
	v_log_f32_e32 v169, v169
	v_cndmask_b32_e32 v166, 0, v232, vcc
	s_mov_b32 s39, 0x3f317217
	v_mul_f32_e32 v171, 0x3f317217, v169
	v_fma_f32 v171, v169, s39, -v171
	v_fmac_f32_e32 v171, 0x3377d1cf, v169
	v_fmac_f32_e32 v171, 0x3f317217, v169
	s_mov_b32 s39, 0x7f800000
	v_cmp_lt_f32_e64 vcc, |v169|, s39
	s_nop 1
	v_cndmask_b32_e32 v169, v169, v171, vcc
	v_sub_f32_e32 v169, v169, v166
	v_fmac_f32_e32 v169, 0x3f317218, v46
	s_mov_b64 exec, s[44:45]
	global_store_dword v167, v169, s[32:33]
	s_mov_b64 exec, -1
	s_cmp_lt_i32 s6, s8
	s_cbranch_scc1 .LatE_loop
.LatE_done:
	s_waitcnt vmcnt(0)
	s_branch .LatE_exit

; #define PH(k, ...) do { if (IN(pb + (k))) { { __VA_ARGS__ } if ((MK_DUP >> (k)) & 1) { xcd_barrier(bar); { __VA_ARGS__ } } } SEAM(pb + (k)); } while (0)
; template <int l> DI void run_layer(const Args& A, LAS unsigned char* lds, const XcdBarrier& bar, int lo, int hi, int G, int bid, int tid, int lane, int wave, int gw, int ngw, int gtid, int nthr) {
;     ...
;     PH(3,
;           if (G > ATT_SCAN_BLK0 && bid >= ATT_SCAN_BLK0) phase_attn(A, lds, 0, ATT_UNITS - ATT_SPLIT, bid - ATT_SCAN_BLK0, G - ATT_SCAN_BLK0, tid, wave, lane);
;           for (int rep = 0; rep < 1 + ((MK_DUP >> 14) & 1); ++rep) for (int u = bid; u < 96; u += G) rwkv_r2_unit(A, lds, u, tid, wave, lane);
;           for (int rep = 0; rep < 1 + ((MK_DUP >> 15) & 1); ++rep) for (int u = bid; u < 96 + 64; u += G) { if (u >= 96) mlstm_m2_unit(A, lds, u - 96, tid, wave, lane); });
.LBB0_2008:
	s_cmp_lt_i32 s6, 15
	s_cselect_b64 s[24:25], -1, 0
	s_and_b64 s[0:1], s[24:25], s[0:1]
	s_andn2_b64 vcc, exec, s[0:1]
	s_cbranch_vccnz .LBB0_2420
	s_cmpk_lt_i32 s50, 0xa1
	s_cselect_b64 s[0:1], -1, 0
	s_cmpk_lt_i32 s92, 0xa0
	s_cselect_b64 s[2:3], -1, 0
	s_or_b64 s[0:1], s[2:3], s[0:1]
	s_and_b64 vcc, exec, s[0:1]
	s_cbranch_vccnz .LBB0_2102
	s_add_i32 s33, s92, 0xffffff60
	s_cmpk_gt_u32 s33, 0x23f
	s_cbranch_scc1 .LBB0_2101
	s_branch .LBB0_2101

; #define LAS __attribute__((address_space(3)))
; DI void attn_unit(const Args& A, LAS unsigned char* lds, int unit, int tid, int wave, int lane) {
;     const bf16* Z = (const bf16*)(A.ws + WS_Z); bf16* ao = (bf16*)(A.ws + WS_ATTO); float* al = (float*)(A.ws + WS_ATTL);
;     const int x = unit & 15; int r0 = unit >> 4; const int hh = r0 & 3; r0 >>= 2; const int b = r0 % NB, br = r0 / NB;
;     const int dil = br == 0 ? 1 : (br == 1 ? 4 : 16), lsub = SEQ / dil, nblk = lsub / 128;
;     const int res = x / nblk, nbk = x % nblk, l0 = nbk * 128, wbase = l0 - 64;
;     LAS bf16* Qs = (LAS bf16*)(lds + AT_QS); LAS bf16* Ks = (LAS bf16*)(lds + AT_KS); LAS bf16* Vt = (LAS bf16*)(lds + AT_VT); LAS float* btab = (LAS float*)(lds + AT_BT);
;     __syncthreads();
; #pragma unroll
;     for (int i = 0; i < 2; ++i) { const int id = tid + 512 * i, row = id >> 3, ch = id & 7; const int tok = b * SEQ + (l0 + row) * dil + res;
;         *(LAS u32x4_t*)(Qs + row * AT_QLD + ch * 8) = *(const u32x4_t*)(Z + (size_t)tok * ZLD + ZA + hh * 64 + ch * 8); }
;     for (int id = tid; id < 272 * 8; id += NTHR) { const int row = id >> 3, ch = id & 7; const int pos = wbase + row; u32x4_t v = (u32x4_t){0u, 0u, 0u, 0u};
;         if (row < 256 && pos >= 0 && pos < lsub) v = *(const u32x4_t*)(Z + (size_t)(b * SEQ + pos * dil + res) * ZLD + ZA + 256 + hh * 64 + ch * 8);
;         *(LAS u32x4_t*)(Ks + row * AT_QLD + ch * 8) = v; }
;     for (int id = tid; id < 272 * 8; id += NTHR) { const int key = id % 272, ch = id / 272; const int pos = wbase + key; u32x4_t v = (u32x4_t){0u, 0u, 0u, 0u};
;         if (key < 256 && pos >= 0 && pos < lsub) v = *(const u32x4_t*)(Z + (size_t)(b * SEQ + pos * dil + res) * ZLD + ZA + 512 + hh * 64 + ch * 8);
;         LAS bf16* d = Vt + (ch * 8) * AT_VLD + key;
;         d[0] = (bf16)(v.x & 0xffffu); d[AT_VLD] = (bf16)(v.x >> 16); d[2 * AT_VLD] = (bf16)(v.y & 0xffffu); d[3 * AT_VLD] = (bf16)(v.y >> 16);
;         d[4 * AT_VLD] = (bf16)(v.z & 0xffffu); d[5 * AT_VLD] = (bf16)(v.z >> 16); d[6 * AT_VLD] = (bf16)(v.w & 0xffffu); d[7 * AT_VLD] = (bf16)(v.w >> 16); }
;     if (tid < 129) btab[tid] = A.in[I_RELB][t5_bucket((tid - 64) * dil) * 4 + hh] * 1.4426950408889634f;
.LBB0_2420:
	v_readlane_b32 s9, v235, 52
	v_readlane_b32 s2, v235, 9
	v_readlane_b32 s3, v235, 10
	v_readlane_b32 s4, v235, 19
	v_readlane_b32 s5, v235, 20
	s_mov_b32 s72, 0x3e38aa3b
	s_mov_b32 s73, 0x3e38aa3b
	v_lshrrev_b32_e32 v2, 3, v0
	v_and_b32_e32 v3, 7, v0
	v_lshlrev_b32_e32 v3, 4, v3
	s_movk_i32 s39, 0x90
	v_mad_u32_u24 v1, v2, s39, v3
	v_and_b32_e32 v5, 0xff, v0
	v_lshrrev_b32_e32 v6, 8, v0
	s_movk_i32 s39, 0x1180
	v_mul_u32_u24_e32 v4, s39, v6
	v_lshl_add_u32 v4, v5, 1, v4
	v_add_u32_e32 v4, 0xe100, v4
	v_lshlrev_b32_e32 v6, 4, v6
	v_lshlrev_b32_e32 v8, 2, v5
	v_add_u32_e32 v8, 0x16d00, v8
	v_subrev_u32_e32 v165, 16, v0
	s_movk_i32 s39, 0x81
	v_cmp_gt_u32_e64 s[42:43], s39, v165
	s_movk_i32 s39, 0xa0
	v_cmp_gt_u32_e64 s[48:49], s39, v0
	v_cmp_gt_u32_e64 s[46:47], 64, v0
	v_cmp_gt_u32_e64 s[44:45], 16, v146
	v_subrev_u32_e32 v165, 0x50, v0
	v_cmp_lt_i32_e32 vcc, 0, v165
	v_mov_b32_e32 v7, 0
	s_nop 0
	v_cndmask_b32_e64 v166, 0, 16, vcc
	v_lshlrev_b32_e32 v167, 0, v165
	v_sub_u32_e32 v168, 0, v167
	v_max_i32_e32 v167, v167, v168
	v_cvt_f32_u32_e32 v168, v167
	v_mul_f32_e32 v168, 0x3e000000, v168
	v_max_f32_e32 v168, 1.0, v168
	v_log_f32_e32 v168, v168
	v_cmp_gt_u32_e32 vcc, 8, v167
	v_mul_f32_e32 v168, 0x3f924925, v168
	v_cvt_i32_f32_e32 v168, v168
	v_min_i32_e32 v168, 7, v168
	v_add_u32_e32 v168, 8, v168
	v_cndmask_b32_e32 v168, v168, v167, vcc
	v_add_u32_e32 v168, v168, v166
	v_lshl_or_b32 v7, v168, 0, v7
	v_lshlrev_b32_e32 v167, 2, v165
	v_sub_u32_e32 v168, 0, v167
	v_max_i32_e32 v167, v167, v168
	v_cvt_f32_u32_e32 v168, v167
	v_mul_f32_e32 v168, 0x3e000000, v168
	v_max_f32_e32 v168, 1.0, v168
	v_log_f32_e32 v168, v168
	v_cmp_gt_u32_e32 vcc, 8, v167
	v_mul_f32_e32 v168, 0x3f924925, v168
	v_cvt_i32_f32_e32 v168, v168
	v_min_i32_e32 v168, 7, v168
	v_add_u32_e32 v168, 8, v168
	v_cndmask_b32_e32 v168, v168, v167, vcc
	v_add_u32_e32 v168, v168, v166
	v_lshl_or_b32 v7, v168, 8, v7
	v_lshlrev_b32_e32 v167, 4, v165
	v_sub_u32_e32 v168, 0, v167
	v_max_i32_e32 v167, v167, v168
	v_cvt_f32_u32_e32 v168, v167
	v_mul_f32_e32 v168, 0x3e000000, v168
	v_max_f32_e32 v168, 1.0, v168
	v_log_f32_e32 v168, v168
	v_cmp_gt_u32_e32 vcc, 8, v167
	v_mul_f32_e32 v168, 0x3f924925, v168
	v_cvt_i32_f32_e32 v168, v168
	v_min_i32_e32 v168, 7, v168
	v_add_u32_e32 v168, 8, v168
	v_cndmask_b32_e32 v168, v168, v167, vcc
	v_add_u32_e32 v168, v168, v166
	v_lshl_or_b32 v7, v168, 16, v7
	v_and_b32_e32 v165, 15, v146
	v_lshrrev_b32_e32 v166, 4, v146
	s_lshl_b32 s39, s9, 4
	v_add_u32_e32 v40, s39, v165
	s_movk_i32 s40, 0x90
	v_mul_u32_u24_e32 v34, s40, v40
	v_lshl_add_u32 v34, v166, 4, v34
	v_lshlrev_b32_e32 v167, 2, v166
	v_sub_u32_e32 v35, v167, v165
	v_lshlrev_b32_e32 v35, 2, v35
	v_add_u32_e32 v35, 0x16d40, v35
	v_add_u32_e32 v167, s39, v167
	v_lshlrev_b32_e32 v36, 2, v167
	v_add_u32_e32 v36, 0x16f80, v36
	s_movk_i32 s40, 0x230
	v_mul_u32_u24_e32 v37, s40, v165
	v_lshl_add_u32 v37, v167, 1, v37
	v_add_u32_e32 v37, 0xe100, v37
	v_add_u32_e32 v9, 0x2300, v37
	v_add_u32_e32 v118, 0x4600, v37
	v_add_u32_e32 v144, 0x6900, v37
	v_xor_b32_e32 v38, 16, v146
	v_lshlrev_b32_e32 v38, 2, v38
	v_xor_b32_e32 v39, 32, v146
	v_lshlrev_b32_e32 v39, 2, v39
	v_lshlrev_b32_e32 v41, 3, v166
	v_mov_b32_e32 v232, 0
	v_mov_b32_e32 v233, 0
	s_movk_i32 s40, 0x230
	v_mul_u32_u24_e32 v168, s40, v0
	v_add_u32_e32 v168, 0xe300, v168
	s_and_saveexec_b64 s[40:41], s[46:47]
	ds_write_b64 v168, v[232:233] offset:0
	ds_write_b64 v168, v[232:233] offset:8
	ds_write_b64 v168, v[232:233] offset:16
	ds_write_b64 v168, v[232:233] offset:24
	s_mov_b64 exec, s[40:41]
	s_add_u32 s88, s2, 0x20040
	s_addc_u32 s89, s3, 0
	s_mov_b32 s90, 0x600
	s_cmp_lg_u32 s9, 0
	s_cbranch_scc1 .LatF_w1
	s_mov_b64 exec, 1
	v_mov_b32_e32 v11, 0
	v_mov_b32_e32 v10, 2
	global_atomic_add v10, v11, v10, s[88:89] sc0
	v_mov_b32_e32 v12, 0x23fa0
	s_waitcnt vmcnt(0)
	ds_write_b32 v12, v10
	s_mov_b64 exec, -1
